# v39 + start-time skew of odd workgroups (s_sleep) in the two norm phases and the in-proj GEMM phase to de-phase bulk memory bursts
# baseline (speedup 1.0000x reference)
.LBB0_113:
	v_readlane_b32 s0, v254, 6
	s_cmp_lt_i32 s0, 2
	v_readlane_b32 s1, v254, 7
	s_cselect_b64 s[6:7], -1, 0
	s_and_b64 s[0:1], s[6:7], s[4:5]
	s_andn2_b64 vcc, exec, s[0:1]
	v_readlane_b32 s2, v254, 8
	v_readlane_b32 s3, v254, 9
	s_cbranch_vccnz .LBB0_121
	v_readlane_b32 s16, v254, 0
	v_readlane_b32 s17, v254, 1
	s_mov_b64 s[12:13], s[16:17]
	s_mov_b64 s[14:15], s[16:17]
	s_mov_b32 s5, 0
	s_mov_b32 s0, 0
	s_cmpk_gt_i32 s68, 0x3ff
	s_cbranch_scc1 .LBB0_121
	s_and_b32 s72, s68, 1
	s_mul_i32 s72, s72, 5
.Lp1skew_loop:
	s_cmp_eq_u32 s72, 0
	s_cbranch_scc1 .Lp1skew_done
	s_sleep 127
	s_sub_u32 s72, s72, 1
	s_branch .Lp1skew_loop
.Lp1skew_done:
	v_mbcnt_lo_u32_b32 v0, -1, s0
	v_readlane_b32 s0, v254, 4
	v_mbcnt_hi_u32_b32 v70, -1, v0
	v_readlane_b32 s1, v254, 5
	v_add_u32_e32 v72, s0, v70
	s_lshl_b32 s0, s68, 4
	s_lshl_b32 s1, s94, 1
	s_load_dwordx2 s[8:9], s[12:13], 0x0
	s_load_dwordx2 s[18:19], s[14:15], 0x20
	s_load_dwordx2 s[10:11], s[16:17], 0x30
	s_add_i32 s2, s1, s0
	s_ashr_i32 s3, s2, 31
	s_lshl_b64 s[2:3], s[2:3], 14
	v_and_b32_e32 v71, 63, v70
	v_mov_b32_e32 v129, 0
	s_waitcnt lgkmcnt(0)
	s_add_u32 s12, s8, s2
	v_lshlrev_b32_e32 v64, 4, v71
	v_mov_b32_e32 v65, v129
	s_addc_u32 s13, s9, s3
	s_waitcnt vmcnt(3)
	v_lshl_add_u64 v[24:25], s[12:13], 0, v[64:65]
	s_movk_i32 s2, 0x1000
	v_add_co_u32_e32 v66, vcc, s2, v24
	s_movk_i32 s3, 0x2000
	s_nop 0
	v_addc_co_u32_e32 v67, vcc, 0, v25, vcc
	v_add_co_u32_e32 v26, vcc, s3, v24
	global_load_dwordx4 v[0:3], v64, s[12:13] offset:1024
	global_load_dwordx4 v[4:7], v64, s[12:13] offset:2048
	v_addc_co_u32_e32 v27, vcc, 0, v25, vcc
	global_load_dwordx4 v[8:11], v64, s[12:13] offset:3072
	global_load_dwordx4 v[12:15], v[26:27], off offset:-4096
	global_load_dwordx4 v[16:19], v[66:67], off offset:1024
	global_load_dwordx4 v[20:23], v[66:67], off offset:2048
	global_load_dwordx4 v[28:31], v[26:27], off
	global_load_dwordx4 v[36:39], v[26:27], off offset:1024
	global_load_dwordx4 v[40:43], v[26:27], off offset:2048
	global_load_dwordx4 v[44:47], v[26:27], off offset:3072
	s_movk_i32 s14, 0x3000
	v_add_co_u32_e32 v68, vcc, s14, v24
	s_or_b32 s4, s1, 1
	s_nop 0
	v_addc_co_u32_e32 v69, vcc, 0, v25, vcc
	global_load_dwordx4 v[32:35], v[66:67], off offset:3072
	global_load_dwordx4 v[48:51], v[68:69], off
	global_load_dwordx4 v[52:55], v[68:69], off offset:1024
	global_load_dwordx4 v[56:59], v[68:69], off offset:2048
	global_load_dwordx4 v[24:27], v64, s[12:13]
	global_load_dwordx4 v[60:63], v[68:69], off offset:3072
	v_lshlrev_b32_e32 v66, 3, v72
	v_ashrrev_i32_e32 v67, 31, v66
	v_lshlrev_b64 v[66:67], 2, v[66:67]
	v_and_b32_e32 v152, 15, v70
	v_lshl_add_u64 v[130:131], s[18:19], 0, v[66:67]
	v_lshl_add_u64 v[68:69], s[48:49], 0, v[66:67]
	v_lshl_add_u64 v[134:135], s[20:21], 0, v[66:67]
	s_mulk_i32 s4, 0x2010
	v_lshlrev_b32_e32 v66, 13, v152
	v_mov_b32_e32 v67, v129
	s_mov_b64 s[12:13], 0x14000
	s_add_i32 s16, s4, 0
	v_lshl_add_u64 v[66:67], s[48:49], 0, v[66:67]
	s_lshl_b32 s4, s94, 10
	v_lshl_add_u64 v[132:133], v[68:69], 0, s[12:13]
	s_mul_i32 s12, s94, 0x4020
	v_lshl_add_u64 v[66:67], v[66:67], 0, s[4:5]
	v_and_b32_e32 v68, 48, v70
	v_mov_b32_e32 v69, v129
	s_add_i32 s15, s12, 0
	v_lshl_add_u64 v[66:67], v[66:67], 0, v[68:69]
	s_mov_b64 s[12:13], 0x270000
	s_add_i32 s5, s4, 0
	s_movk_i32 s17, 0x2010
	v_lshl_add_u64 v[136:137], v[66:67], 0, s[12:13]
	v_mov_b32_e32 v66, s5
	s_add_i32 s12, 0, 0x20100
	v_mad_u32_u24 v69, v152, s17, v66
	s_add_i32 s4, s12, s4
	v_and_b32_e32 v66, 0x300, v64
	v_lshlrev_b32_e32 v67, 2, v152
	v_add3_u32 v153, s4, v66, v67
	v_ashrrev_i32_e32 v66, 4, v72
	v_lshlrev_b32_e32 v67, 6, v152
	v_lshlrev_b32_e32 v70, 2, v66
	v_add3_u32 v154, s12, v67, v70
	v_ashrrev_i32_e32 v67, 31, v66
	v_lshl_add_u64 v[138:139], v[66:67], 2, s[10:11]
	v_lshlrev_b64 v[66:67], 14, v[66:67]
	v_lshlrev_b32_e32 v128, 2, v71
	v_lshl_add_u64 v[66:67], s[48:49], 0, v[66:67]
	s_mov_b64 s[10:11], 0x70000
	v_lshl_add_u64 v[140:141], v[66:67], 0, s[10:11]
	v_lshl_add_u64 v[142:143], s[8:9], 0, v[64:65]
	v_lshl_add_u64 v[64:65], s[48:49], 0, v[128:129]
	s_mov_b64 s[10:11], 0x49400000
	v_lshl_add_u64 v[144:145], v[64:65], 0, s[10:11]
	s_movk_i32 s4, 0x100
	v_lshlrev_b32_e32 v155, 3, v71
	s_lshl_b32 s17, s46, 4
	v_mbcnt_lo_u32_b32 v64, -1, 0
	v_lshlrev_b32_e32 v149, 4, v72
	v_cmp_gt_i32_e64 s[4:5], s4, v72
	v_or_b32_e32 v156, 0x200, v155
	v_or_b32_e32 v157, 0x400, v155
	v_or_b32_e32 v158, 0x600, v155
	v_or_b32_e32 v159, 0x800, v155
	v_or_b32_e32 v160, 0xa00, v155
	v_or_b32_e32 v161, 0xc00, v155
	v_or_b32_e32 v162, 0xe00, v155
	v_or_b32_e32 v163, 0x1000, v155
	v_or_b32_e32 v164, 0x1200, v155
	v_or_b32_e32 v165, 0x1400, v155
	v_or_b32_e32 v166, 0x1600, v155
	v_or_b32_e32 v167, 0x1800, v155
	v_or_b32_e32 v168, 0x1a00, v155
	v_or_b32_e32 v169, 0x1c00, v155
	v_or_b32_e32 v170, 0x1e00, v155
	s_add_i32 s18, s17, s1
	s_add_i32 s19, 0, 0x22100
	s_add_i32 s20, 0, 0x24100
	v_mov_b32_e32 v129, 0x358637bd
	v_add_u32_e32 v171, v69, v68
	s_mov_b32 s21, 0xbfb8aa3b
	s_mov_b32 s22, 0x3f2aaaab
	v_mov_b32_e32 v172, 0x3ecc95a3
	s_mov_b32 s23, 0x3f317218
	s_mov_b32 s24, 0x7f800000
	s_mov_b32 s25, 0x33800000
	v_mov_b32_e32 v173, 0x18000
	v_mbcnt_hi_u32_b32 v174, -1, v64
	v_mov_b32_e32 v146, 0x3f317218
	v_mov_b32_e32 v175, 0x7f800000
	v_mov_b32_e32 v176, 0x7fc00000
	v_mov_b32_e32 v177, 0xff800000
	s_mov_b32 s26, s68
	s_branch .LBB0_117

.LBB0_168:
	s_and_b32 s72, s68, 1
	s_mul_i32 s72, s72, 4

.LBB0_616:
	v_readlane_b32 s0, v254, 6
	v_readlane_b32 s1, v254, 7
	s_cmp_lt_i32 s0, 6
	v_readlane_b32 s0, v254, 0
	v_readlane_b32 s1, v254, 1
	s_load_dwordx2 s[0:1], s[0:1], 0xa0
	v_readlane_b32 s2, v254, 8
	v_readlane_b32 s3, v254, 9
	s_cselect_b64 s[4:5], -1, 0
	s_waitcnt lgkmcnt(0)
	s_add_u32 s0, s0, 0x400000
	s_addc_u32 s1, s1, 0
	s_and_b64 s[2:3], s[4:5], s[8:9]
	s_andn2_b64 vcc, exec, s[2:3]
	s_cbranch_vccnz .LBB0_622
	v_readlane_b32 s8, v254, 0
	v_readlane_b32 s9, v254, 1
	s_mov_b32 s2, 0
	s_cmpk_gt_i32 s68, 0x3ff
	s_cbranch_scc1 .LBB0_622
	s_and_b32 s72, s68, 1
	s_mul_i32 s72, s72, 4

.Lp5skew_done:
	v_readlane_b32 s6, v254, 0
	v_readlane_b32 s7, v254, 1
	s_load_dwordx2 s[12:13], s[6:7], 0xa0
	v_mbcnt_lo_u32_b32 v0, -1, s2
	v_mbcnt_hi_u32_b32 v4, -1, v0
	v_and_b32_e32 v6, 63, v4
	s_waitcnt vmcnt(0)
	v_mov_b32_e32 v25, 0
	s_waitcnt lgkmcnt(0)
	s_add_u32 s6, s12, 0x4d400000
	s_addc_u32 s7, s13, 0
	s_lshl_b32 s2, s68, 4
	s_lshl_b32 s3, s94, 1
	s_add_i32 s10, s3, s2
	s_ashr_i32 s11, s10, 31
	s_lshl_b64 s[10:11], s[10:11], 13
	s_add_u32 s10, s6, s10
	v_lshlrev_b32_e32 v0, 3, v6
	v_mov_b32_e32 v1, v25
	s_addc_u32 s11, s7, s11
	v_lshl_add_u64 v[2:3], s[10:11], 0, v[0:1]
	s_movk_i32 s14, 0x1000
	v_add_co_u32_e32 v2, vcc, s14, v2
	s_load_dwordx2 s[8:9], s[8:9], 0x68
	s_nop 0
	v_addc_co_u32_e32 v3, vcc, 0, v3, vcc
	global_load_dwordx2 v[26:27], v0, s[10:11]
	global_load_dwordx2 v[28:29], v0, s[10:11] offset:512
	global_load_dwordx2 v[30:31], v0, s[10:11] offset:1024
	global_load_dwordx2 v[32:33], v0, s[10:11] offset:1536
	global_load_dwordx2 v[34:35], v0, s[10:11] offset:2048
	global_load_dwordx2 v[36:37], v0, s[10:11] offset:2560
	global_load_dwordx2 v[38:39], v0, s[10:11] offset:3072
	global_load_dwordx2 v[40:41], v0, s[10:11] offset:3584
	global_load_dwordx2 v[48:49], v[2:3], off
	global_load_dwordx2 v[50:51], v[2:3], off offset:512
	global_load_dwordx2 v[52:53], v[2:3], off offset:1024
	global_load_dwordx2 v[54:55], v[2:3], off offset:1536
	global_load_dwordx2 v[56:57], v[2:3], off offset:2048
	global_load_dwordx2 v[58:59], v[2:3], off offset:2560
	global_load_dwordx2 v[60:61], v[2:3], off offset:3072
	global_load_dwordx2 v[62:63], v[2:3], off offset:3584
	s_lshl_b32 s10, s94, 9
	v_lshl_add_u32 v2, v4, 3, s10
	v_ashrrev_i32_e32 v3, 31, v2
	v_lshlrev_b64 v[4:5], 2, v[2:3]
	s_waitcnt lgkmcnt(0)
	v_lshl_add_u64 v[42:43], s[8:9], 0, v[4:5]
	v_lshl_add_u64 v[4:5], s[12:13], 0, v[4:5]
	s_mov_b64 s[8:9], 0x20000
	v_lshlrev_b32_e32 v3, 2, v2
	v_mbcnt_lo_u32_b32 v2, -1, 0
	v_lshl_add_u64 v[44:45], v[4:5], 0, s[8:9]
	s_mov_b64 s[8:9], 0x1c000
	v_mbcnt_hi_u32_b32 v2, -1, v2
	v_lshl_add_u64 v[46:47], v[4:5], 0, s[8:9]
	v_and_b32_e32 v4, 64, v2
	v_add_u32_e32 v4, 64, v4
	v_xor_b32_e32 v5, 32, v2
	v_cmp_lt_i32_e32 vcc, v5, v4
	v_lshlrev_b32_e32 v24, 2, v6
	v_lshlrev_b32_e32 v170, 4, v6
	v_cndmask_b32_e32 v5, v2, v5, vcc
	v_lshlrev_b32_e32 v164, 2, v5
	v_xor_b32_e32 v5, 16, v2
	v_cmp_lt_i32_e32 vcc, v5, v4
	v_or_b32_e32 v6, 0xa00, v24
	v_or_b32_e32 v8, 0xb00, v24
	v_cndmask_b32_e32 v5, v2, v5, vcc
	v_lshlrev_b32_e32 v165, 2, v5
	v_xor_b32_e32 v5, 8, v2
	v_cmp_lt_i32_e32 vcc, v5, v4
	v_or_b32_e32 v10, 0xc00, v24
	v_or_b32_e32 v12, 0xd00, v24
	v_cndmask_b32_e32 v5, v2, v5, vcc
	v_lshlrev_b32_e32 v166, 2, v5
	v_xor_b32_e32 v5, 4, v2
	v_cmp_lt_i32_e32 vcc, v5, v4
	v_or_b32_e32 v14, 0xe00, v24
	v_or_b32_e32 v16, 0xf00, v24
	v_cndmask_b32_e32 v5, v2, v5, vcc
	v_lshlrev_b32_e32 v167, 2, v5
	v_xor_b32_e32 v5, 2, v2
	v_cmp_lt_i32_e32 vcc, v5, v4
	v_lshl_add_u64 v[64:65], s[6:7], 0, v[0:1]
	v_lshl_add_u64 v[0:1], s[12:13], 0, v[24:25]
	v_cndmask_b32_e32 v5, v2, v5, vcc
	v_lshlrev_b32_e32 v168, 2, v5
	v_xor_b32_e32 v5, 1, v2
	v_cmp_lt_i32_e32 vcc, v5, v4
	v_or_b32_e32 v4, 0x900, v24
	s_mov_b64 s[8:9], 0x49400000
	v_cndmask_b32_e32 v2, v2, v5, vcc
	v_lshlrev_b32_e32 v169, 2, v2
	v_or_b32_e32 v2, 0x800, v24
	v_or_b32_e32 v5, 0x400, v170
	v_or_b32_e32 v7, 0x800, v170
	v_or_b32_e32 v9, 0xc00, v170
	v_or_b32_e32 v11, 0x1000, v170
	v_or_b32_e32 v13, 0x1400, v170
	v_or_b32_e32 v15, 0x1800, v170
	v_or_b32_e32 v17, 0x1c00, v170
	v_lshlrev_b32_e32 v18, 2, v2
	v_lshlrev_b32_e32 v19, 2, v4
	v_lshlrev_b32_e32 v20, 2, v6
	v_lshlrev_b32_e32 v21, 2, v8
	v_lshlrev_b32_e32 v22, 2, v10
	v_lshlrev_b32_e32 v23, 2, v12
	v_lshlrev_b32_e32 v68, 2, v14
	v_lshlrev_b32_e32 v69, 2, v16
	v_lshl_add_u64 v[66:67], v[0:1], 0, s[8:9]
	s_add_i32 s8, s68, s64
	s_lshl_b32 s15, s8, 4
	s_lshl_b32 s16, s64, 4
	v_add_u32_e32 v25, 0, v3
	v_mov_b32_e32 v171, 0x358637bd
	v_lshlrev_b32_e32 v172, 1, v2
	v_lshlrev_b32_e32 v173, 1, v4
	v_lshlrev_b32_e32 v174, 1, v6
	v_lshlrev_b32_e32 v175, 1, v8
	v_lshlrev_b32_e32 v176, 1, v10
	v_lshlrev_b32_e32 v177, 1, v12
	v_lshlrev_b32_e32 v178, 1, v14
	v_lshlrev_b32_e32 v179, 1, v16
	v_mov_b32_e32 v180, 0x18000
	v_add_u32_e32 v181, 0, v5
	v_add_u32_e32 v182, 0, v7
	v_add_u32_e32 v183, 0, v9
	v_add_u32_e32 v184, 0, v11
	v_add_u32_e32 v185, 0, v13
	v_add_u32_e32 v186, 0, v15
	v_add_u32_e32 v187, 0, v17
	v_add_u32_e32 v188, 0, v18
	v_add_u32_e32 v189, 0, v19
	v_add_u32_e32 v190, 0, v20
	v_add_u32_e32 v191, 0, v21
	v_add_u32_e32 v192, 0, v22
	v_add_u32_e32 v193, 0, v23
	v_add_u32_e32 v194, 0, v68
	v_add_u32_e32 v195, 0, v69
	s_mov_b32 s17, s68
	s_branch .LBB0_620
